# barrier-wait conversion: waves stop taking new items once 2 of the 8 XCCs have arrived (was: half of them), on top of best
# baseline (speedup 1.0000x reference)
; __device__ __forceinline__ unsigned xb_ld(unsigned* p)              { return __hip_atomic_load(p, __ATOMIC_RELAXED, __HIP_MEMORY_SCOPE_AGENT); }
;     ...
;     for (;;) {
;         unsigned f = 0u; if (lane < 16) f = xb_ld(&bar[XB_FLAG(lane)]);
;         const bool waiting = (lane < 16) && ((mask >> lane) & 1u) && ((int)(f - gen) <= 0);
;         const unsigned long long wm = __builtin_amdgcn_ballot_w64(waiting);
;         if (wm == 0ull) break;
;         if (stopw && 2 * __builtin_popcountll(wm) <= __builtin_popcount(mask)) { *stopw = stopv; stopw = nullptr; }
;         __builtin_amdgcn_s_sleep(1);
;         if ((++sp & 255u) == 0u) { if (xb_ld(&bar[XB_TMO])) break; if (sp > XB_SPIN_CAP) { if (lane == 0) atomicAdd(&bar[XB_TMO], 1u); break; } }
;     }
.LBB0_244:
	s_or_b64 exec, exec, s[14:15]
	v_cndmask_b32_e64 v5, 0, 1, s[16:17]
	v_cmp_ne_u32_e32 vcc, 0, v5
	s_or_b64 s[12:13], s[12:13], exec
	s_cbranch_vccz .LBB0_252
	s_cmp_eq_u32 s18, 0
	s_mov_b32 s24, 0
	s_cbranch_scc1 .LBB0_249
	s_bcnt1_i32_b64 s14, vcc
	s_nop 0
	v_cmp_gt_u32_e64 vcc, s14, 6
	s_cbranch_vccnz .LBB0_248
	v_mov_b32_e32 v5, s18
	s_mov_b32 s18, 0
	ds_write_b32 v5, v4
